# B5 EpiMoeDown TOK/GATE loads issued at epilogue start under per-row-group exec masks, one wait
# speedup vs baseline: 1.0136x; 1.0098x over previous
.LBB0_1670:
	s_nop 15
	s_nop 7
	s_lshl_b32 s33, s54, 13
	s_lshl_b32 s55, s62, 8
	s_add_i32 s55, s55, s33
	v_cmp_gt_i32_e32 vcc, s63, v165
	s_and_saveexec_b64 s[0:1], vcc
	v_add_u32_e32 v2, s55, v165
	v_ashrrev_i32_e32 v3, 31, v2
	v_lshlrev_b64 v[2:3], 2, v[2:3]
	v_lshl_add_u64 v[4:5], s[64:65], 0, v[2:3]
	v_lshl_add_u64 v[2:3], s[34:35], 0, v[2:3]
	global_load_dword v14, v[4:5], off
	global_load_dword v15, v[2:3], off
	s_or_b64 exec, exec, s[0:1]
	v_cmp_gt_i32_e32 vcc, s63, v166
	s_and_saveexec_b64 s[0:1], vcc
	v_add_u32_e32 v2, s55, v166
	v_ashrrev_i32_e32 v3, 31, v2
	v_lshlrev_b64 v[2:3], 2, v[2:3]
	v_lshl_add_u64 v[4:5], s[64:65], 0, v[2:3]
	v_lshl_add_u64 v[2:3], s[34:35], 0, v[2:3]
	global_load_dword v16, v[4:5], off
	global_load_dword v17, v[2:3], off
	s_or_b64 exec, exec, s[0:1]
	v_cmp_gt_i32_e32 vcc, s63, v167
	s_and_saveexec_b64 s[0:1], vcc
	v_add_u32_e32 v2, s55, v167
	v_ashrrev_i32_e32 v3, 31, v2
	v_lshlrev_b64 v[2:3], 2, v[2:3]
	v_lshl_add_u64 v[4:5], s[64:65], 0, v[2:3]
	v_lshl_add_u64 v[2:3], s[34:35], 0, v[2:3]
	global_load_dword v18, v[4:5], off
	global_load_dword v19, v[2:3], off
	s_or_b64 exec, exec, s[0:1]
	v_cmp_gt_i32_e32 vcc, s63, v182
	s_and_saveexec_b64 s[0:1], vcc
	v_add_u32_e32 v2, s55, v182
	v_ashrrev_i32_e32 v3, 31, v2
	v_lshlrev_b64 v[2:3], 2, v[2:3]
	v_lshl_add_u64 v[4:5], s[64:65], 0, v[2:3]
	v_lshl_add_u64 v[2:3], s[34:35], 0, v[2:3]
	global_load_dword v20, v[4:5], off
	global_load_dword v21, v[2:3], off
	s_or_b64 exec, exec, s[0:1]
	v_cmp_gt_i32_e32 vcc, s63, v183
	s_and_saveexec_b64 s[0:1], vcc
	v_add_u32_e32 v2, s55, v183
	v_ashrrev_i32_e32 v3, 31, v2
	v_lshlrev_b64 v[2:3], 2, v[2:3]
	v_lshl_add_u64 v[4:5], s[64:65], 0, v[2:3]
	v_lshl_add_u64 v[2:3], s[34:35], 0, v[2:3]
	global_load_dword v22, v[4:5], off
	global_load_dword v23, v[2:3], off
	s_or_b64 exec, exec, s[0:1]
	v_cmp_gt_i32_e32 vcc, s63, v184
	s_and_saveexec_b64 s[0:1], vcc
	v_add_u32_e32 v2, s55, v184
	v_ashrrev_i32_e32 v3, 31, v2
	v_lshlrev_b64 v[2:3], 2, v[2:3]
	v_lshl_add_u64 v[4:5], s[64:65], 0, v[2:3]
	v_lshl_add_u64 v[2:3], s[34:35], 0, v[2:3]
	global_load_dword v24, v[4:5], off
	global_load_dword v25, v[2:3], off
	s_or_b64 exec, exec, s[0:1]
	v_cmp_gt_i32_e32 vcc, s63, v185
	s_and_saveexec_b64 s[0:1], vcc
	v_add_u32_e32 v2, s55, v185
	v_ashrrev_i32_e32 v3, 31, v2
	v_lshlrev_b64 v[2:3], 2, v[2:3]
	v_lshl_add_u64 v[4:5], s[64:65], 0, v[2:3]
	v_lshl_add_u64 v[2:3], s[34:35], 0, v[2:3]
	global_load_dword v26, v[4:5], off
	global_load_dword v27, v[2:3], off
	s_or_b64 exec, exec, s[0:1]
	v_cmp_gt_i32_e32 vcc, s63, v186
	s_and_saveexec_b64 s[0:1], vcc
	v_add_u32_e32 v2, s55, v186
	v_ashrrev_i32_e32 v3, 31, v2
	v_lshlrev_b64 v[2:3], 2, v[2:3]
	v_lshl_add_u64 v[4:5], s[64:65], 0, v[2:3]
	v_lshl_add_u64 v[2:3], s[34:35], 0, v[2:3]
	global_load_dword v28, v[4:5], off
	global_load_dword v29, v[2:3], off
	s_or_b64 exec, exec, s[0:1]
	v_cmp_gt_i32_e32 vcc, s63, v165
	v_lshlrev_b32_e32 v0, 1, v160
	s_and_saveexec_b64 s[0:1], vcc
	s_cbranch_execz .LBB0_1679
	s_lshl_b32 s33, s54, 13
	s_lshl_b32 s55, s62, 8
	s_add_i32 s55, s55, s33
	v_add_u32_e32 v2, s55, v165
	v_ashrrev_i32_e32 v3, 31, v2
	v_lshlrev_b64 v[2:3], 2, v[2:3]
	v_lshl_add_u64 v[4:5], s[64:65], 0, v[2:3]
	v_lshl_add_u64 v[2:3], s[34:35], 0, v[2:3]
	s_waitcnt vmcnt(0)
	s_lshl_b32 s80, s61, 8
	v_mov_b32_e32 v1, v14
	s_ashr_i32 s81, s80, 31
	v_mov_b32_e32 v2, v15
	v_mul_f32_e32 v6, 0x3d000000, v2
	v_lshlrev_b32_e32 v2, 13, v1
	v_and_b32_e32 v172, 0x2000, v2
	v_ashrrev_i32_e32 v2, 1, v1
	v_ashrrev_i32_e32 v3, 31, v2
	v_lshl_add_u64 v[2:3], v[172:173], 0, v[2:3]
	v_lshlrev_b64 v[2:3], 12, v[2:3]
	v_lshl_add_u64 v[2:3], s[22:23], 0, v[2:3]
	v_lshl_add_u64 v[2:3], s[80:81], 1, v[2:3]
	s_lshl_b32 s80, s53, 1
	s_mov_b32 s81, s60
	v_lshl_add_u64 v[2:3], v[2:3], 0, s[80:81]
	v_mov_b32_e32 v1, v173
	v_lshl_add_u64 v[8:9], v[2:3], 0, v[0:1]
	v_pk_mul_f32 v[4:5], v[158:159], v[6:7] op_sel_hi:[1,0]
	v_pk_mul_f32 v[2:3], v[156:157], v[6:7] op_sel_hi:[1,0]
	v_pk_mul_f32 v[10:11], v[154:155], v[6:7] op_sel_hi:[1,0]
	v_pk_mul_f32 v[12:13], v[152:153], v[6:7] op_sel_hi:[1,0]
	v_cvt_pk_bf16_f32 v2, v2, v3
	v_cvt_pk_bf16_f32 v3, v4, v5
	s_nop 0
	v_cvt_pk_bf16_f32 v4, v12, v13
	v_cvt_pk_bf16_f32 v5, v10, v11
	global_store_dwordx4 v[8:9], v[2:5], off
	v_pk_mul_f32 v[10:11], v[146:147], v[6:7] op_sel_hi:[1,0]
	s_nop 0
	v_pk_mul_f32 v[4:5], v[150:151], v[6:7] op_sel_hi:[1,0]
	v_pk_mul_f32 v[2:3], v[148:149], v[6:7] op_sel_hi:[1,0]
	v_pk_mul_f32 v[6:7], v[144:145], v[6:7] op_sel_hi:[1,0]
	v_cvt_pk_bf16_f32 v2, v2, v3
	v_cvt_pk_bf16_f32 v3, v4, v5
	s_nop 0
	v_cvt_pk_bf16_f32 v4, v6, v7
	v_cvt_pk_bf16_f32 v5, v10, v11
	global_store_dwordx4 v[8:9], v[2:5], off offset:256
	s_or_b64 exec, exec, s[0:1]
	v_cmp_gt_i32_e32 vcc, s63, v166
	s_and_saveexec_b64 s[0:1], vcc
	s_cbranch_execnz .LBB0_1680

.LBB0_1673:
	s_lshl_b32 s33, s54, 13
	s_lshl_b32 s55, s62, 8
	s_add_i32 s55, s55, s33
	v_add_u32_e32 v2, s55, v167
	v_ashrrev_i32_e32 v3, 31, v2
	v_lshlrev_b64 v[2:3], 2, v[2:3]
	v_lshl_add_u64 v[4:5], s[64:65], 0, v[2:3]
	v_lshl_add_u64 v[2:3], s[34:35], 0, v[2:3]
	s_nop 0
	s_lshl_b32 s80, s61, 8
	v_mov_b32_e32 v1, v18
	s_ashr_i32 s81, s80, 31
	v_mov_b32_e32 v2, v19
	v_mul_f32_e32 v6, 0x3d000000, v2
	v_lshlrev_b32_e32 v2, 13, v1
	v_and_b32_e32 v172, 0x2000, v2
	v_ashrrev_i32_e32 v2, 1, v1
	v_ashrrev_i32_e32 v3, 31, v2
	v_lshl_add_u64 v[2:3], v[172:173], 0, v[2:3]
	v_lshlrev_b64 v[2:3], 12, v[2:3]
	v_lshl_add_u64 v[2:3], s[22:23], 0, v[2:3]
	v_lshl_add_u64 v[2:3], s[80:81], 1, v[2:3]
	s_lshl_b32 s80, s53, 1
	s_mov_b32 s81, s60
	v_lshl_add_u64 v[2:3], v[2:3], 0, s[80:81]
	v_mov_b32_e32 v1, v173
	v_lshl_add_u64 v[8:9], v[2:3], 0, v[0:1]
	v_pk_mul_f32 v[4:5], v[126:127], v[6:7] op_sel_hi:[1,0]
	v_pk_mul_f32 v[2:3], v[124:125], v[6:7] op_sel_hi:[1,0]
	v_pk_mul_f32 v[10:11], v[122:123], v[6:7] op_sel_hi:[1,0]
	v_pk_mul_f32 v[12:13], v[120:121], v[6:7] op_sel_hi:[1,0]
	v_cvt_pk_bf16_f32 v2, v2, v3
	v_cvt_pk_bf16_f32 v3, v4, v5
	s_nop 0
	v_cvt_pk_bf16_f32 v4, v12, v13
	v_cvt_pk_bf16_f32 v5, v10, v11
	global_store_dwordx4 v[8:9], v[2:5], off
	v_pk_mul_f32 v[10:11], v[114:115], v[6:7] op_sel_hi:[1,0]
	s_nop 0
	v_pk_mul_f32 v[4:5], v[118:119], v[6:7] op_sel_hi:[1,0]
	v_pk_mul_f32 v[2:3], v[116:117], v[6:7] op_sel_hi:[1,0]
	v_pk_mul_f32 v[6:7], v[112:113], v[6:7] op_sel_hi:[1,0]
	v_cvt_pk_bf16_f32 v2, v2, v3
	v_cvt_pk_bf16_f32 v3, v4, v5
	s_nop 0
	v_cvt_pk_bf16_f32 v4, v6, v7
	v_cvt_pk_bf16_f32 v5, v10, v11
	global_store_dwordx4 v[8:9], v[2:5], off offset:256
	s_or_b64 exec, exec, s[0:1]
	v_cmp_gt_i32_e32 vcc, s63, v182
	s_and_saveexec_b64 s[0:1], vcc
	s_cbranch_execnz .LBB0_1682

.LBB0_1675:
	s_lshl_b32 s33, s54, 13
	s_lshl_b32 s55, s62, 8
	s_add_i32 s55, s55, s33
	v_add_u32_e32 v2, s55, v183
	v_ashrrev_i32_e32 v3, 31, v2
	v_lshlrev_b64 v[2:3], 2, v[2:3]
	v_lshl_add_u64 v[4:5], s[64:65], 0, v[2:3]
	v_lshl_add_u64 v[2:3], s[34:35], 0, v[2:3]
	s_nop 0
	s_lshl_b32 s80, s61, 8
	v_mov_b32_e32 v1, v22
	s_ashr_i32 s81, s80, 31
	v_mov_b32_e32 v2, v23
	v_mul_f32_e32 v6, 0x3d000000, v2
	v_lshlrev_b32_e32 v2, 13, v1
	v_and_b32_e32 v172, 0x2000, v2
	v_ashrrev_i32_e32 v2, 1, v1
	v_ashrrev_i32_e32 v3, 31, v2
	v_lshl_add_u64 v[2:3], v[172:173], 0, v[2:3]
	v_lshlrev_b64 v[2:3], 12, v[2:3]
	v_lshl_add_u64 v[2:3], s[22:23], 0, v[2:3]
	v_lshl_add_u64 v[2:3], s[80:81], 1, v[2:3]
	s_lshl_b32 s80, s53, 1
	s_mov_b32 s81, s60
	v_lshl_add_u64 v[2:3], v[2:3], 0, s[80:81]
	v_mov_b32_e32 v1, v173
	v_lshl_add_u64 v[8:9], v[2:3], 0, v[0:1]
	v_pk_mul_f32 v[4:5], v[94:95], v[6:7] op_sel_hi:[1,0]
	v_pk_mul_f32 v[2:3], v[92:93], v[6:7] op_sel_hi:[1,0]
	v_pk_mul_f32 v[10:11], v[90:91], v[6:7] op_sel_hi:[1,0]
	v_pk_mul_f32 v[12:13], v[88:89], v[6:7] op_sel_hi:[1,0]
	v_cvt_pk_bf16_f32 v2, v2, v3
	v_cvt_pk_bf16_f32 v3, v4, v5
	s_nop 0
	v_cvt_pk_bf16_f32 v4, v12, v13
	v_cvt_pk_bf16_f32 v5, v10, v11
	global_store_dwordx4 v[8:9], v[2:5], off
	v_pk_mul_f32 v[10:11], v[82:83], v[6:7] op_sel_hi:[1,0]
	s_nop 0
	v_pk_mul_f32 v[4:5], v[86:87], v[6:7] op_sel_hi:[1,0]
	v_pk_mul_f32 v[2:3], v[84:85], v[6:7] op_sel_hi:[1,0]
	v_pk_mul_f32 v[6:7], v[80:81], v[6:7] op_sel_hi:[1,0]
	v_cvt_pk_bf16_f32 v2, v2, v3
	v_cvt_pk_bf16_f32 v3, v4, v5
	s_nop 0
	v_cvt_pk_bf16_f32 v4, v6, v7
	v_cvt_pk_bf16_f32 v5, v10, v11
	global_store_dwordx4 v[8:9], v[2:5], off offset:256
	s_or_b64 exec, exec, s[0:1]
	v_cmp_gt_i32_e32 vcc, s63, v184
	s_and_saveexec_b64 s[0:1], vcc
	s_cbranch_execnz .LBB0_1684

.LBB0_1677:
	s_lshl_b32 s33, s54, 13
	s_lshl_b32 s55, s62, 8
	s_add_i32 s55, s55, s33
	v_add_u32_e32 v2, s55, v185
	v_ashrrev_i32_e32 v3, 31, v2
	v_lshlrev_b64 v[2:3], 2, v[2:3]
	v_lshl_add_u64 v[4:5], s[64:65], 0, v[2:3]
	v_lshl_add_u64 v[2:3], s[34:35], 0, v[2:3]
	s_nop 0
	s_lshl_b32 s80, s61, 8
	v_mov_b32_e32 v1, v26
	s_ashr_i32 s81, s80, 31
	v_mov_b32_e32 v2, v27
	v_mul_f32_e32 v6, 0x3d000000, v2
	v_lshlrev_b32_e32 v2, 13, v1
	v_and_b32_e32 v172, 0x2000, v2
	v_ashrrev_i32_e32 v2, 1, v1
	v_ashrrev_i32_e32 v3, 31, v2
	v_lshl_add_u64 v[2:3], v[172:173], 0, v[2:3]
	v_lshlrev_b64 v[2:3], 12, v[2:3]
	v_lshl_add_u64 v[2:3], s[22:23], 0, v[2:3]
	v_lshl_add_u64 v[2:3], s[80:81], 1, v[2:3]
	s_lshl_b32 s80, s53, 1
	s_mov_b32 s81, s60
	v_lshl_add_u64 v[2:3], v[2:3], 0, s[80:81]
	v_mov_b32_e32 v1, v173
	v_lshl_add_u64 v[8:9], v[2:3], 0, v[0:1]
	v_pk_mul_f32 v[4:5], v[62:63], v[6:7] op_sel_hi:[1,0]
	v_pk_mul_f32 v[2:3], v[60:61], v[6:7] op_sel_hi:[1,0]
	v_pk_mul_f32 v[10:11], v[58:59], v[6:7] op_sel_hi:[1,0]
	v_pk_mul_f32 v[12:13], v[56:57], v[6:7] op_sel_hi:[1,0]
	v_cvt_pk_bf16_f32 v2, v2, v3
	v_cvt_pk_bf16_f32 v3, v4, v5
	s_nop 0
	v_cvt_pk_bf16_f32 v4, v12, v13
	v_cvt_pk_bf16_f32 v5, v10, v11
	global_store_dwordx4 v[8:9], v[2:5], off
	v_pk_mul_f32 v[10:11], v[50:51], v[6:7] op_sel_hi:[1,0]
	s_nop 0
	v_pk_mul_f32 v[4:5], v[54:55], v[6:7] op_sel_hi:[1,0]
	v_pk_mul_f32 v[2:3], v[52:53], v[6:7] op_sel_hi:[1,0]
	v_pk_mul_f32 v[6:7], v[48:49], v[6:7] op_sel_hi:[1,0]
	v_cvt_pk_bf16_f32 v2, v2, v3
	v_cvt_pk_bf16_f32 v3, v4, v5
	s_nop 0
	v_cvt_pk_bf16_f32 v4, v6, v7
	v_cvt_pk_bf16_f32 v5, v10, v11
	global_store_dwordx4 v[8:9], v[2:5], off offset:256
	s_or_b64 exec, exec, s[0:1]
	v_cmp_gt_i32_e32 vcc, s63, v186
	s_and_saveexec_b64 s[0:1], vcc
	s_cbranch_execnz .LBB0_1686

.LBB0_1680:
	s_lshl_b32 s33, s54, 13
	s_lshl_b32 s55, s62, 8
	s_add_i32 s55, s55, s33
	v_add_u32_e32 v2, s55, v166
	v_ashrrev_i32_e32 v3, 31, v2
	v_lshlrev_b64 v[2:3], 2, v[2:3]
	v_lshl_add_u64 v[4:5], s[64:65], 0, v[2:3]
	v_lshl_add_u64 v[2:3], s[34:35], 0, v[2:3]
	s_nop 0
	s_lshl_b32 s80, s61, 8
	v_mov_b32_e32 v1, v16
	s_ashr_i32 s81, s80, 31
	v_mov_b32_e32 v2, v17
	v_mul_f32_e32 v6, 0x3d000000, v2
	v_lshlrev_b32_e32 v2, 13, v1
	v_and_b32_e32 v172, 0x2000, v2
	v_ashrrev_i32_e32 v2, 1, v1
	v_ashrrev_i32_e32 v3, 31, v2
	v_lshl_add_u64 v[2:3], v[172:173], 0, v[2:3]
	v_lshlrev_b64 v[2:3], 12, v[2:3]
	v_lshl_add_u64 v[2:3], s[22:23], 0, v[2:3]
	v_lshl_add_u64 v[2:3], s[80:81], 1, v[2:3]
	s_lshl_b32 s80, s53, 1
	s_mov_b32 s81, s60
	v_lshl_add_u64 v[2:3], v[2:3], 0, s[80:81]
	v_mov_b32_e32 v1, v173
	v_lshl_add_u64 v[8:9], v[2:3], 0, v[0:1]
	v_pk_mul_f32 v[4:5], v[142:143], v[6:7] op_sel_hi:[1,0]
	v_pk_mul_f32 v[2:3], v[140:141], v[6:7] op_sel_hi:[1,0]
	v_pk_mul_f32 v[10:11], v[138:139], v[6:7] op_sel_hi:[1,0]
	v_pk_mul_f32 v[12:13], v[136:137], v[6:7] op_sel_hi:[1,0]
	v_cvt_pk_bf16_f32 v2, v2, v3
	v_cvt_pk_bf16_f32 v3, v4, v5
	s_nop 0
	v_cvt_pk_bf16_f32 v4, v12, v13
	v_cvt_pk_bf16_f32 v5, v10, v11
	global_store_dwordx4 v[8:9], v[2:5], off
	v_pk_mul_f32 v[10:11], v[130:131], v[6:7] op_sel_hi:[1,0]
	s_nop 0
	v_pk_mul_f32 v[4:5], v[134:135], v[6:7] op_sel_hi:[1,0]
	v_pk_mul_f32 v[2:3], v[132:133], v[6:7] op_sel_hi:[1,0]
	v_pk_mul_f32 v[6:7], v[128:129], v[6:7] op_sel_hi:[1,0]
	v_cvt_pk_bf16_f32 v2, v2, v3
	v_cvt_pk_bf16_f32 v3, v4, v5
	s_nop 0
	v_cvt_pk_bf16_f32 v4, v6, v7
	v_cvt_pk_bf16_f32 v5, v10, v11
	global_store_dwordx4 v[8:9], v[2:5], off offset:256
	s_or_b64 exec, exec, s[0:1]
	v_cmp_gt_i32_e32 vcc, s63, v167
	s_and_saveexec_b64 s[0:1], vcc
	s_cbranch_execnz .LBB0_1673

.LBB0_1682:
	s_lshl_b32 s33, s54, 13
	s_lshl_b32 s55, s62, 8
	s_add_i32 s55, s55, s33
	v_add_u32_e32 v2, s55, v182
	v_ashrrev_i32_e32 v3, 31, v2
	v_lshlrev_b64 v[2:3], 2, v[2:3]
	v_lshl_add_u64 v[4:5], s[64:65], 0, v[2:3]
	v_lshl_add_u64 v[2:3], s[34:35], 0, v[2:3]
	s_nop 0
	s_lshl_b32 s80, s61, 8
	v_mov_b32_e32 v1, v20
	s_ashr_i32 s81, s80, 31
	v_mov_b32_e32 v2, v21
	v_mul_f32_e32 v6, 0x3d000000, v2
	v_lshlrev_b32_e32 v2, 13, v1
	v_and_b32_e32 v172, 0x2000, v2
	v_ashrrev_i32_e32 v2, 1, v1
	v_ashrrev_i32_e32 v3, 31, v2
	v_lshl_add_u64 v[2:3], v[172:173], 0, v[2:3]
	v_lshlrev_b64 v[2:3], 12, v[2:3]
	v_lshl_add_u64 v[2:3], s[22:23], 0, v[2:3]
	v_lshl_add_u64 v[2:3], s[80:81], 1, v[2:3]
	s_lshl_b32 s80, s53, 1
	s_mov_b32 s81, s60
	v_lshl_add_u64 v[2:3], v[2:3], 0, s[80:81]
	v_mov_b32_e32 v1, v173
	v_lshl_add_u64 v[8:9], v[2:3], 0, v[0:1]
	v_pk_mul_f32 v[4:5], v[110:111], v[6:7] op_sel_hi:[1,0]
	v_pk_mul_f32 v[2:3], v[108:109], v[6:7] op_sel_hi:[1,0]
	v_pk_mul_f32 v[10:11], v[106:107], v[6:7] op_sel_hi:[1,0]
	v_pk_mul_f32 v[12:13], v[104:105], v[6:7] op_sel_hi:[1,0]
	v_cvt_pk_bf16_f32 v2, v2, v3
	v_cvt_pk_bf16_f32 v3, v4, v5
	s_nop 0
	v_cvt_pk_bf16_f32 v4, v12, v13
	v_cvt_pk_bf16_f32 v5, v10, v11
	global_store_dwordx4 v[8:9], v[2:5], off
	v_pk_mul_f32 v[10:11], v[98:99], v[6:7] op_sel_hi:[1,0]
	s_nop 0
	v_pk_mul_f32 v[4:5], v[102:103], v[6:7] op_sel_hi:[1,0]
	v_pk_mul_f32 v[2:3], v[100:101], v[6:7] op_sel_hi:[1,0]
	v_pk_mul_f32 v[6:7], v[96:97], v[6:7] op_sel_hi:[1,0]
	v_cvt_pk_bf16_f32 v2, v2, v3
	v_cvt_pk_bf16_f32 v3, v4, v5
	s_nop 0
	v_cvt_pk_bf16_f32 v4, v6, v7
	v_cvt_pk_bf16_f32 v5, v10, v11
	global_store_dwordx4 v[8:9], v[2:5], off offset:256
	s_or_b64 exec, exec, s[0:1]
	v_cmp_gt_i32_e32 vcc, s63, v183
	s_and_saveexec_b64 s[0:1], vcc
	s_cbranch_execnz .LBB0_1675

.LBB0_1684:
	s_lshl_b32 s33, s54, 13
	s_lshl_b32 s55, s62, 8
	s_add_i32 s55, s55, s33
	v_add_u32_e32 v2, s55, v184
	v_ashrrev_i32_e32 v3, 31, v2
	v_lshlrev_b64 v[2:3], 2, v[2:3]
	v_lshl_add_u64 v[4:5], s[64:65], 0, v[2:3]
	v_lshl_add_u64 v[2:3], s[34:35], 0, v[2:3]
	s_nop 0
	s_lshl_b32 s80, s61, 8
	v_mov_b32_e32 v1, v24
	s_ashr_i32 s81, s80, 31
	v_mov_b32_e32 v2, v25
	v_mul_f32_e32 v6, 0x3d000000, v2
	v_lshlrev_b32_e32 v2, 13, v1
	v_and_b32_e32 v172, 0x2000, v2
	v_ashrrev_i32_e32 v2, 1, v1
	v_ashrrev_i32_e32 v3, 31, v2
	v_lshl_add_u64 v[2:3], v[172:173], 0, v[2:3]
	v_lshlrev_b64 v[2:3], 12, v[2:3]
	v_lshl_add_u64 v[2:3], s[22:23], 0, v[2:3]
	v_lshl_add_u64 v[2:3], s[80:81], 1, v[2:3]
	s_lshl_b32 s80, s53, 1
	s_mov_b32 s81, s60
	v_lshl_add_u64 v[2:3], v[2:3], 0, s[80:81]
	v_mov_b32_e32 v1, v173
	v_lshl_add_u64 v[8:9], v[2:3], 0, v[0:1]
	v_pk_mul_f32 v[4:5], v[78:79], v[6:7] op_sel_hi:[1,0]
	v_pk_mul_f32 v[2:3], v[76:77], v[6:7] op_sel_hi:[1,0]
	v_pk_mul_f32 v[10:11], v[74:75], v[6:7] op_sel_hi:[1,0]
	v_pk_mul_f32 v[12:13], v[72:73], v[6:7] op_sel_hi:[1,0]
	v_cvt_pk_bf16_f32 v2, v2, v3
	v_cvt_pk_bf16_f32 v3, v4, v5
	s_nop 0
	v_cvt_pk_bf16_f32 v4, v12, v13
	v_cvt_pk_bf16_f32 v5, v10, v11
	global_store_dwordx4 v[8:9], v[2:5], off
	v_pk_mul_f32 v[10:11], v[66:67], v[6:7] op_sel_hi:[1,0]
	s_nop 0
	v_pk_mul_f32 v[4:5], v[70:71], v[6:7] op_sel_hi:[1,0]
	v_pk_mul_f32 v[2:3], v[68:69], v[6:7] op_sel_hi:[1,0]
	v_pk_mul_f32 v[6:7], v[64:65], v[6:7] op_sel_hi:[1,0]
	v_cvt_pk_bf16_f32 v2, v2, v3
	v_cvt_pk_bf16_f32 v3, v4, v5
	s_nop 0
	v_cvt_pk_bf16_f32 v4, v6, v7
	v_cvt_pk_bf16_f32 v5, v10, v11
	global_store_dwordx4 v[8:9], v[2:5], off offset:256
	s_or_b64 exec, exec, s[0:1]
	v_cmp_gt_i32_e32 vcc, s63, v185
	s_and_saveexec_b64 s[0:1], vcc
	s_cbranch_execnz .LBB0_1677

.LBB0_1686:
	s_lshl_b32 s33, s54, 13
	s_lshl_b32 s54, s62, 8
	s_add_i32 s54, s54, s33
	v_add_u32_e32 v2, s54, v186
	v_ashrrev_i32_e32 v3, 31, v2
	v_lshlrev_b64 v[2:3], 2, v[2:3]
	v_lshl_add_u64 v[4:5], s[64:65], 0, v[2:3]
	v_lshl_add_u64 v[2:3], s[34:35], 0, v[2:3]
	s_nop 0
	s_lshl_b32 s54, s61, 8
	v_mov_b32_e32 v1, v28
	s_ashr_i32 s55, s54, 31
	v_mov_b32_e32 v2, v29
	v_mul_f32_e32 v4, 0x3d000000, v2
	v_lshlrev_b32_e32 v2, 13, v1
	v_and_b32_e32 v172, 0x2000, v2
	v_ashrrev_i32_e32 v2, 1, v1
	v_ashrrev_i32_e32 v3, 31, v2
	v_lshl_add_u64 v[2:3], v[172:173], 0, v[2:3]
	v_lshlrev_b64 v[2:3], 12, v[2:3]
	v_lshl_add_u64 v[2:3], s[22:23], 0, v[2:3]
	v_lshl_add_u64 v[2:3], s[54:55], 1, v[2:3]
	s_lshl_b32 s54, s53, 1
	s_mov_b32 s55, s60
	v_lshl_add_u64 v[2:3], v[2:3], 0, s[54:55]
	v_mov_b32_e32 v1, v173
	v_lshl_add_u64 v[6:7], v[2:3], 0, v[0:1]
	v_pk_mul_f32 v[2:3], v[46:47], v[4:5] op_sel_hi:[1,0]
	v_pk_mul_f32 v[0:1], v[44:45], v[4:5] op_sel_hi:[1,0]
	v_pk_mul_f32 v[8:9], v[42:43], v[4:5] op_sel_hi:[1,0]
	v_pk_mul_f32 v[10:11], v[40:41], v[4:5] op_sel_hi:[1,0]
	v_cvt_pk_bf16_f32 v0, v0, v1
	v_cvt_pk_bf16_f32 v1, v2, v3
	s_nop 0
	v_cvt_pk_bf16_f32 v2, v10, v11
	v_cvt_pk_bf16_f32 v3, v8, v9
	global_store_dwordx4 v[6:7], v[0:3], off
	v_pk_mul_f32 v[8:9], v[34:35], v[4:5] op_sel_hi:[1,0]
	s_nop 0
	v_pk_mul_f32 v[2:3], v[38:39], v[4:5] op_sel_hi:[1,0]
	v_pk_mul_f32 v[0:1], v[36:37], v[4:5] op_sel_hi:[1,0]
	v_pk_mul_f32 v[4:5], v[32:33], v[4:5] op_sel_hi:[1,0]
	v_cvt_pk_bf16_f32 v0, v0, v1
	v_cvt_pk_bf16_f32 v1, v2, v3
	s_nop 0
	v_cvt_pk_bf16_f32 v2, v4, v5
	v_cvt_pk_bf16_f32 v3, v8, v9
	global_store_dwordx4 v[6:7], v[0:3], off offset:256
	s_or_b64 exec, exec, s[0:1]
	s_andn2_b64 vcc, exec, s[36:37]
	s_mov_b64 s[0:1], -1
	s_cbranch_vccnz .LBB0_1661
